# K3 fast copy: row strides folded into offset immediates (one scalar base bump per two rows)
# speedup vs baseline: 1.0081x; 1.0081x over previous
_Z20refine_gather_kernelPKfS0_S0_S0_S0_S0_S0_PfPiS1_:
	s_load_dwordx16 s[4:19], s[0:1], 0x0
	s_load_dwordx4 s[20:23], s[0:1], 0x40
	v_and_b32_e32 v1, 63, v0
	s_bfe_u32 s24, s2, 0x30003
	s_lshr_b32 s25, s2, 6
	s_lshl_b32 s25, s25, 2
	s_bfe_u32 s26, s2, 0x20001
	s_or_b32 s25, s25, s26
	s_and_b32 s26, s2, 1
	v_lshlrev_b32_e32 v2, 5, v1
	v_lshl_or_b32 v2, s24, 11, v2
	s_waitcnt lgkmcnt(0)
	s_load_dword s27, s[14:15], 0x0
	global_load_dwordx4 v[4:7], v2, s[16:17]
	global_load_dwordx4 v[8:11], v2, s[16:17] offset:16
	s_cmp_eq_u32 s26, 0
	s_cselect_b32 s30, s4, s6
	s_cselect_b32 s31, s5, s7
	s_lshl_b32 s32, s24, 5
	s_add_i32 s32, s32, s25
	s_lshl_b32 s32, s32, 18
	s_lshl_b32 s33, s26, 26
	s_or_b32 s32, s32, s33
	s_add_u32 s34, s22, s32
	s_addc_u32 s35, s23, 0
	v_mov_b32_e32 v18, 0
	v_mov_b32_e32 v19, 0x7f800000
	s_waitcnt vmcnt(0) lgkmcnt(0)
	v_add_f32_e32 v12, v4, v5
	v_add_f32_e32 v13, v6, v7
	v_add_f32_e32 v14, v8, v9
	v_add_f32_e32 v15, v10, v11
	v_add_f32_e32 v12, v12, v13
	v_add_f32_e32 v14, v14, v15
	v_add_f32_e32 v12, v12, v14
	v_mov_b32_e32 v3, s27
	v_fmamk_f32 v3, v12, 0x3c800000, v3
	v_add_f32_e32 v16, 0xba03126f, v3
	v_add_f32_e32 v17, 0x3a03126f, v3
	v_readlane_b32 s40, v3, 0
	v_readlane_b32 s41, v3, 1
	v_readlane_b32 s42, v3, 2
	v_readlane_b32 s43, v3, 3
	v_readlane_b32 s44, v3, 4
	v_readlane_b32 s45, v3, 5
	v_readlane_b32 s46, v3, 6
	v_readlane_b32 s47, v3, 7
	v_cmp_gt_f32_e64 s[48:49], s40, v3
	v_cmp_gt_f32_e64 s[50:51], s41, v3
	v_cmp_gt_f32_e64 s[52:53], s42, v3
	v_cmp_gt_f32_e64 s[54:55], s43, v3
	v_cmp_gt_f32_e64 s[56:57], s44, v3
	v_cmp_gt_f32_e64 s[58:59], s45, v3
	v_cmp_gt_f32_e64 s[60:61], s46, v3
	v_cmp_gt_f32_e64 s[62:63], s47, v3
	v_addc_co_u32_e64 v18, vcc, 0, v18, s[48:49]
	v_addc_co_u32_e64 v18, vcc, 0, v18, s[50:51]
	v_addc_co_u32_e64 v18, vcc, 0, v18, s[52:53]
	v_addc_co_u32_e64 v18, vcc, 0, v18, s[54:55]
	v_addc_co_u32_e64 v18, vcc, 0, v18, s[56:57]
	v_addc_co_u32_e64 v18, vcc, 0, v18, s[58:59]
	v_addc_co_u32_e64 v18, vcc, 0, v18, s[60:61]
	v_addc_co_u32_e64 v18, vcc, 0, v18, s[62:63]
	v_readlane_b32 s40, v3, 8
	v_readlane_b32 s41, v3, 9
	v_readlane_b32 s42, v3, 10
	v_readlane_b32 s43, v3, 11
	v_readlane_b32 s44, v3, 12
	v_readlane_b32 s45, v3, 13
	v_readlane_b32 s46, v3, 14
	v_readlane_b32 s47, v3, 15
	v_cmp_gt_f32_e64 s[48:49], s40, v3
	v_cmp_gt_f32_e64 s[50:51], s41, v3
	v_cmp_gt_f32_e64 s[52:53], s42, v3
	v_cmp_gt_f32_e64 s[54:55], s43, v3
	v_cmp_gt_f32_e64 s[56:57], s44, v3
	v_cmp_gt_f32_e64 s[58:59], s45, v3
	v_cmp_gt_f32_e64 s[60:61], s46, v3
	v_cmp_gt_f32_e64 s[62:63], s47, v3
	v_addc_co_u32_e64 v18, vcc, 0, v18, s[48:49]
	v_addc_co_u32_e64 v18, vcc, 0, v18, s[50:51]
	v_addc_co_u32_e64 v18, vcc, 0, v18, s[52:53]
	v_addc_co_u32_e64 v18, vcc, 0, v18, s[54:55]
	v_addc_co_u32_e64 v18, vcc, 0, v18, s[56:57]
	v_addc_co_u32_e64 v18, vcc, 0, v18, s[58:59]
	v_addc_co_u32_e64 v18, vcc, 0, v18, s[60:61]
	v_addc_co_u32_e64 v18, vcc, 0, v18, s[62:63]
	v_readlane_b32 s40, v3, 16
	v_readlane_b32 s41, v3, 17
	v_readlane_b32 s42, v3, 18
	v_readlane_b32 s43, v3, 19
	v_readlane_b32 s44, v3, 20
	v_readlane_b32 s45, v3, 21
	v_readlane_b32 s46, v3, 22
	v_readlane_b32 s47, v3, 23
	v_cmp_gt_f32_e64 s[48:49], s40, v3
	v_cmp_gt_f32_e64 s[50:51], s41, v3
	v_cmp_gt_f32_e64 s[52:53], s42, v3
	v_cmp_gt_f32_e64 s[54:55], s43, v3
	v_cmp_gt_f32_e64 s[56:57], s44, v3
	v_cmp_gt_f32_e64 s[58:59], s45, v3
	v_cmp_gt_f32_e64 s[60:61], s46, v3
	v_cmp_gt_f32_e64 s[62:63], s47, v3
	v_addc_co_u32_e64 v18, vcc, 0, v18, s[48:49]
	v_addc_co_u32_e64 v18, vcc, 0, v18, s[50:51]
	v_addc_co_u32_e64 v18, vcc, 0, v18, s[52:53]
	v_addc_co_u32_e64 v18, vcc, 0, v18, s[54:55]
	v_addc_co_u32_e64 v18, vcc, 0, v18, s[56:57]
	v_addc_co_u32_e64 v18, vcc, 0, v18, s[58:59]
	v_addc_co_u32_e64 v18, vcc, 0, v18, s[60:61]
	v_addc_co_u32_e64 v18, vcc, 0, v18, s[62:63]
	v_readlane_b32 s40, v3, 24
	v_readlane_b32 s41, v3, 25
	v_readlane_b32 s42, v3, 26
	v_readlane_b32 s43, v3, 27
	v_readlane_b32 s44, v3, 28
	v_readlane_b32 s45, v3, 29
	v_readlane_b32 s46, v3, 30
	v_readlane_b32 s47, v3, 31
	v_cmp_gt_f32_e64 s[48:49], s40, v3
	v_cmp_gt_f32_e64 s[50:51], s41, v3
	v_cmp_gt_f32_e64 s[52:53], s42, v3
	v_cmp_gt_f32_e64 s[54:55], s43, v3
	v_cmp_gt_f32_e64 s[56:57], s44, v3
	v_cmp_gt_f32_e64 s[58:59], s45, v3
	v_cmp_gt_f32_e64 s[60:61], s46, v3
	v_cmp_gt_f32_e64 s[62:63], s47, v3
	v_addc_co_u32_e64 v18, vcc, 0, v18, s[48:49]
	v_addc_co_u32_e64 v18, vcc, 0, v18, s[50:51]
	v_addc_co_u32_e64 v18, vcc, 0, v18, s[52:53]
	v_addc_co_u32_e64 v18, vcc, 0, v18, s[54:55]
	v_addc_co_u32_e64 v18, vcc, 0, v18, s[56:57]
	v_addc_co_u32_e64 v18, vcc, 0, v18, s[58:59]
	v_addc_co_u32_e64 v18, vcc, 0, v18, s[60:61]
	v_addc_co_u32_e64 v18, vcc, 0, v18, s[62:63]
	v_readlane_b32 s40, v3, 32
	v_readlane_b32 s41, v3, 33
	v_readlane_b32 s42, v3, 34
	v_readlane_b32 s43, v3, 35
	v_readlane_b32 s44, v3, 36
	v_readlane_b32 s45, v3, 37
	v_readlane_b32 s46, v3, 38
	v_readlane_b32 s47, v3, 39
	v_cmp_gt_f32_e64 s[48:49], s40, v3
	v_cmp_gt_f32_e64 s[50:51], s41, v3
	v_cmp_gt_f32_e64 s[52:53], s42, v3
	v_cmp_gt_f32_e64 s[54:55], s43, v3
	v_cmp_gt_f32_e64 s[56:57], s44, v3
	v_cmp_gt_f32_e64 s[58:59], s45, v3
	v_cmp_gt_f32_e64 s[60:61], s46, v3
	v_cmp_gt_f32_e64 s[62:63], s47, v3
	v_addc_co_u32_e64 v18, vcc, 0, v18, s[48:49]
	v_addc_co_u32_e64 v18, vcc, 0, v18, s[50:51]
	v_addc_co_u32_e64 v18, vcc, 0, v18, s[52:53]
	v_addc_co_u32_e64 v18, vcc, 0, v18, s[54:55]
	v_addc_co_u32_e64 v18, vcc, 0, v18, s[56:57]
	v_addc_co_u32_e64 v18, vcc, 0, v18, s[58:59]
	v_addc_co_u32_e64 v18, vcc, 0, v18, s[60:61]
	v_addc_co_u32_e64 v18, vcc, 0, v18, s[62:63]
	v_readlane_b32 s40, v3, 40
	v_readlane_b32 s41, v3, 41
	v_readlane_b32 s42, v3, 42
	v_readlane_b32 s43, v3, 43
	v_readlane_b32 s44, v3, 44
	v_readlane_b32 s45, v3, 45
	v_readlane_b32 s46, v3, 46
	v_readlane_b32 s47, v3, 47
	v_cmp_gt_f32_e64 s[48:49], s40, v3
	v_cmp_gt_f32_e64 s[50:51], s41, v3
	v_cmp_gt_f32_e64 s[52:53], s42, v3
	v_cmp_gt_f32_e64 s[54:55], s43, v3
	v_cmp_gt_f32_e64 s[56:57], s44, v3
	v_cmp_gt_f32_e64 s[58:59], s45, v3
	v_cmp_gt_f32_e64 s[60:61], s46, v3
	v_cmp_gt_f32_e64 s[62:63], s47, v3
	v_addc_co_u32_e64 v18, vcc, 0, v18, s[48:49]
	v_addc_co_u32_e64 v18, vcc, 0, v18, s[50:51]
	v_addc_co_u32_e64 v18, vcc, 0, v18, s[52:53]
	v_addc_co_u32_e64 v18, vcc, 0, v18, s[54:55]
	v_addc_co_u32_e64 v18, vcc, 0, v18, s[56:57]
	v_addc_co_u32_e64 v18, vcc, 0, v18, s[58:59]
	v_addc_co_u32_e64 v18, vcc, 0, v18, s[60:61]
	v_addc_co_u32_e64 v18, vcc, 0, v18, s[62:63]
	v_readlane_b32 s40, v3, 48
	v_readlane_b32 s41, v3, 49
	v_readlane_b32 s42, v3, 50
	v_readlane_b32 s43, v3, 51
	v_readlane_b32 s44, v3, 52
	v_readlane_b32 s45, v3, 53
	v_readlane_b32 s46, v3, 54
	v_readlane_b32 s47, v3, 55
	v_cmp_gt_f32_e64 s[48:49], s40, v3
	v_cmp_gt_f32_e64 s[50:51], s41, v3
	v_cmp_gt_f32_e64 s[52:53], s42, v3
	v_cmp_gt_f32_e64 s[54:55], s43, v3
	v_cmp_gt_f32_e64 s[56:57], s44, v3
	v_cmp_gt_f32_e64 s[58:59], s45, v3
	v_cmp_gt_f32_e64 s[60:61], s46, v3
	v_cmp_gt_f32_e64 s[62:63], s47, v3
	v_addc_co_u32_e64 v18, vcc, 0, v18, s[48:49]
	v_addc_co_u32_e64 v18, vcc, 0, v18, s[50:51]
	v_addc_co_u32_e64 v18, vcc, 0, v18, s[52:53]
	v_addc_co_u32_e64 v18, vcc, 0, v18, s[54:55]
	v_addc_co_u32_e64 v18, vcc, 0, v18, s[56:57]
	v_addc_co_u32_e64 v18, vcc, 0, v18, s[58:59]
	v_addc_co_u32_e64 v18, vcc, 0, v18, s[60:61]
	v_addc_co_u32_e64 v18, vcc, 0, v18, s[62:63]
	v_readlane_b32 s40, v3, 56
	v_readlane_b32 s41, v3, 57
	v_readlane_b32 s42, v3, 58
	v_readlane_b32 s43, v3, 59
	v_readlane_b32 s44, v3, 60
	v_readlane_b32 s45, v3, 61
	v_readlane_b32 s46, v3, 62
	v_readlane_b32 s47, v3, 63
	v_cmp_gt_f32_e64 s[48:49], s40, v3
	v_cmp_gt_f32_e64 s[50:51], s41, v3
	v_cmp_gt_f32_e64 s[52:53], s42, v3
	v_cmp_gt_f32_e64 s[54:55], s43, v3
	v_cmp_gt_f32_e64 s[56:57], s44, v3
	v_cmp_gt_f32_e64 s[58:59], s45, v3
	v_cmp_gt_f32_e64 s[60:61], s46, v3
	v_cmp_gt_f32_e64 s[62:63], s47, v3
	v_addc_co_u32_e64 v18, vcc, 0, v18, s[48:49]
	v_addc_co_u32_e64 v18, vcc, 0, v18, s[50:51]
	v_addc_co_u32_e64 v18, vcc, 0, v18, s[52:53]
	v_addc_co_u32_e64 v18, vcc, 0, v18, s[54:55]
	v_addc_co_u32_e64 v18, vcc, 0, v18, s[56:57]
	v_addc_co_u32_e64 v18, vcc, 0, v18, s[58:59]
	v_addc_co_u32_e64 v18, vcc, 0, v18, s[60:61]
	v_addc_co_u32_e64 v18, vcc, 0, v18, s[62:63]
	v_cmp_gt_u32_e64 s[48:49], 32, v18
	v_cmp_gt_u32_e64 s[50:51], 33, v18
	s_nop 1
	v_cndmask_b32_e64 v20, v19, v3, s[48:49]
	v_cndmask_b32_e64 v21, v19, v3, s[50:51]
	s_nop 1
	v_min_f32_dpp v20, v20, v20 quad_perm:[1,0,3,2] row_mask:0xf bank_mask:0xf
	v_min_f32_dpp v21, v21, v21 quad_perm:[1,0,3,2] row_mask:0xf bank_mask:0xf
	s_nop 1
	v_min_f32_dpp v20, v20, v20 quad_perm:[2,3,0,1] row_mask:0xf bank_mask:0xf
	v_min_f32_dpp v21, v21, v21 quad_perm:[2,3,0,1] row_mask:0xf bank_mask:0xf
	s_nop 1
	v_min_f32_dpp v20, v20, v20 row_half_mirror row_mask:0xf bank_mask:0xf
	v_min_f32_dpp v21, v21, v21 row_half_mirror row_mask:0xf bank_mask:0xf
	s_nop 1
	v_min_f32_dpp v20, v20, v20 row_mirror row_mask:0xf bank_mask:0xf
	v_min_f32_dpp v21, v21, v21 row_mirror row_mask:0xf bank_mask:0xf
	s_nop 1
	v_readlane_b32 s40, v20, 0
	v_readlane_b32 s41, v20, 16
	v_readlane_b32 s42, v20, 32
	v_readlane_b32 s43, v20, 48
	v_readlane_b32 s44, v21, 0
	v_readlane_b32 s45, v21, 16
	v_readlane_b32 s46, v21, 32
	v_readlane_b32 s47, v21, 48
	v_mov_b32_e32 v22, s40
	v_mov_b32_e32 v23, s44
	v_min_f32_e32 v22, s41, v22
	v_min_f32_e32 v23, s45, v23
	v_min_f32_e32 v22, s42, v22
	v_min_f32_e32 v23, s46, v23
	v_min_f32_e32 v22, s43, v22
	v_min_f32_e32 v23, s47, v23
	v_cmp_lt_f32_e64 s[50:51], v23, v16
	v_cmp_gt_f32_e64 s[52:53], v22, v17
	s_or_b64 s[54:55], s[50:51], s[52:53]
	s_not_b64 s[54:55], s[54:55]
	s_cbranch_scc1 .Lrg_slow
	v_mbcnt_lo_u32_b32 v22, s50, 0
	v_mbcnt_hi_u32_b32 v22, s51, v22
	v_cmp_eq_u32_e64 s[56:57], s25, v22
	s_and_b64 s[56:57], s[56:57], s[50:51]
	s_ff1_i32_b64 s28, s[56:57]
	s_lshl_b32 s29, s24, 6
	s_add_i32 s29, s29, s28
	s_lshl_b32 s29, s29, 18
	s_add_u32 s30, s30, s29
	s_addc_u32 s31, s31, 0
	v_lshlrev_b32_e32 v2, 4, v0
	s_add_u32 s30, s30, 0x1000
	s_addc_u32 s31, s31, 0
	s_add_u32 s34, s34, 0x1000
	s_addc_u32 s35, s35, 0
	global_load_dwordx4 v[4:7], v2, s[30:31] offset:-4096 nt
	global_load_dwordx4 v[8:11], v2, s[30:31] nt
	s_add_u32 s30, s30, 0x2000
	s_addc_u32 s31, s31, 0
	global_load_dwordx4 v[12:15], v2, s[30:31] offset:-4096 nt
	global_load_dwordx4 v[16:19], v2, s[30:31] nt
	s_add_u32 s30, s30, 0x2000
	s_addc_u32 s31, s31, 0
	global_load_dwordx4 v[20:23], v2, s[30:31] offset:-4096 nt
	global_load_dwordx4 v[24:27], v2, s[30:31] nt
	s_add_u32 s30, s30, 0x2000
	s_addc_u32 s31, s31, 0
	global_load_dwordx4 v[28:31], v2, s[30:31] offset:-4096 nt
	global_load_dwordx4 v[32:35], v2, s[30:31] nt
	s_add_u32 s30, s30, 0x2000
	s_addc_u32 s31, s31, 0
	s_waitcnt vmcnt(7)
	global_store_dwordx4 v2, v[4:7], s[34:35] offset:-4096 nt
	s_nop 0
	global_load_dwordx4 v[4:7], v2, s[30:31] offset:-4096 nt
	s_waitcnt vmcnt(8)
	global_store_dwordx4 v2, v[8:11], s[34:35] nt
	s_add_u32 s34, s34, 0x2000
	s_addc_u32 s35, s35, 0
	global_load_dwordx4 v[8:11], v2, s[30:31] nt
	s_add_u32 s30, s30, 0x2000
	s_addc_u32 s31, s31, 0
	s_waitcnt vmcnt(9)
	global_store_dwordx4 v2, v[12:15], s[34:35] offset:-4096 nt
	s_nop 0
	global_load_dwordx4 v[12:15], v2, s[30:31] offset:-4096 nt
	s_waitcnt vmcnt(10)
	global_store_dwordx4 v2, v[16:19], s[34:35] nt
	s_add_u32 s34, s34, 0x2000
	s_addc_u32 s35, s35, 0
	global_load_dwordx4 v[16:19], v2, s[30:31] nt
	s_add_u32 s30, s30, 0x2000
	s_addc_u32 s31, s31, 0
	s_waitcnt vmcnt(11)
	global_store_dwordx4 v2, v[20:23], s[34:35] offset:-4096 nt
	s_nop 0
	global_load_dwordx4 v[20:23], v2, s[30:31] offset:-4096 nt
	s_waitcnt vmcnt(12)
	global_store_dwordx4 v2, v[24:27], s[34:35] nt
	s_add_u32 s34, s34, 0x2000
	s_addc_u32 s35, s35, 0
	global_load_dwordx4 v[24:27], v2, s[30:31] nt
	s_add_u32 s30, s30, 0x2000
	s_addc_u32 s31, s31, 0
	s_waitcnt vmcnt(13)
	global_store_dwordx4 v2, v[28:31], s[34:35] offset:-4096 nt
	s_nop 0
	global_load_dwordx4 v[28:31], v2, s[30:31] offset:-4096 nt
	s_waitcnt vmcnt(14)
	global_store_dwordx4 v2, v[32:35], s[34:35] nt
	s_add_u32 s34, s34, 0x2000
	s_addc_u32 s35, s35, 0
	global_load_dwordx4 v[32:35], v2, s[30:31] nt
	s_add_u32 s30, s30, 0x2000
	s_addc_u32 s31, s31, 0
	s_waitcnt vmcnt(14)
	global_store_dwordx4 v2, v[4:7], s[34:35] offset:-4096 nt
	s_nop 0
	global_load_dwordx4 v[4:7], v2, s[30:31] offset:-4096 nt
	s_waitcnt vmcnt(14)
	global_store_dwordx4 v2, v[8:11], s[34:35] nt
	s_add_u32 s34, s34, 0x2000
	s_addc_u32 s35, s35, 0
	global_load_dwordx4 v[8:11], v2, s[30:31] nt
	s_add_u32 s30, s30, 0x2000
	s_addc_u32 s31, s31, 0
	s_waitcnt vmcnt(14)
	global_store_dwordx4 v2, v[12:15], s[34:35] offset:-4096 nt
	s_nop 0
	global_load_dwordx4 v[12:15], v2, s[30:31] offset:-4096 nt
	s_waitcnt vmcnt(14)
	global_store_dwordx4 v2, v[16:19], s[34:35] nt
	s_add_u32 s34, s34, 0x2000
	s_addc_u32 s35, s35, 0
	global_load_dwordx4 v[16:19], v2, s[30:31] nt
	s_add_u32 s30, s30, 0x2000
	s_addc_u32 s31, s31, 0
	s_waitcnt vmcnt(14)
	global_store_dwordx4 v2, v[20:23], s[34:35] offset:-4096 nt
	s_nop 0
	global_load_dwordx4 v[20:23], v2, s[30:31] offset:-4096 nt
	s_waitcnt vmcnt(14)
	global_store_dwordx4 v2, v[24:27], s[34:35] nt
	s_add_u32 s34, s34, 0x2000
	s_addc_u32 s35, s35, 0
	global_load_dwordx4 v[24:27], v2, s[30:31] nt
	s_add_u32 s30, s30, 0x2000
	s_addc_u32 s31, s31, 0
	s_waitcnt vmcnt(14)
	global_store_dwordx4 v2, v[28:31], s[34:35] offset:-4096 nt
	s_nop 0
	global_load_dwordx4 v[28:31], v2, s[30:31] offset:-4096 nt
	s_waitcnt vmcnt(14)
	global_store_dwordx4 v2, v[32:35], s[34:35] nt
	s_add_u32 s34, s34, 0x2000
	s_addc_u32 s35, s35, 0
	global_load_dwordx4 v[32:35], v2, s[30:31] nt
	s_add_u32 s30, s30, 0x2000
	s_addc_u32 s31, s31, 0
	s_waitcnt vmcnt(14)
	global_store_dwordx4 v2, v[4:7], s[34:35] offset:-4096 nt
	s_nop 0
	global_load_dwordx4 v[4:7], v2, s[30:31] offset:-4096 nt
	s_waitcnt vmcnt(14)
	global_store_dwordx4 v2, v[8:11], s[34:35] nt
	s_add_u32 s34, s34, 0x2000
	s_addc_u32 s35, s35, 0
	global_load_dwordx4 v[8:11], v2, s[30:31] nt
	s_add_u32 s30, s30, 0x2000
	s_addc_u32 s31, s31, 0
	s_waitcnt vmcnt(14)
	global_store_dwordx4 v2, v[12:15], s[34:35] offset:-4096 nt
	s_nop 0
	global_load_dwordx4 v[12:15], v2, s[30:31] offset:-4096 nt
	s_waitcnt vmcnt(14)
	global_store_dwordx4 v2, v[16:19], s[34:35] nt
	s_add_u32 s34, s34, 0x2000
	s_addc_u32 s35, s35, 0
	global_load_dwordx4 v[16:19], v2, s[30:31] nt
	s_add_u32 s30, s30, 0x2000
	s_addc_u32 s31, s31, 0
	s_waitcnt vmcnt(14)
	global_store_dwordx4 v2, v[20:23], s[34:35] offset:-4096 nt
	s_nop 0
	global_load_dwordx4 v[20:23], v2, s[30:31] offset:-4096 nt
	s_waitcnt vmcnt(14)
	global_store_dwordx4 v2, v[24:27], s[34:35] nt
	s_add_u32 s34, s34, 0x2000
	s_addc_u32 s35, s35, 0
	global_load_dwordx4 v[24:27], v2, s[30:31] nt
	s_add_u32 s30, s30, 0x2000
	s_addc_u32 s31, s31, 0
	s_waitcnt vmcnt(14)
	global_store_dwordx4 v2, v[28:31], s[34:35] offset:-4096 nt
	s_nop 0
	global_load_dwordx4 v[28:31], v2, s[30:31] offset:-4096 nt
	s_waitcnt vmcnt(14)
	global_store_dwordx4 v2, v[32:35], s[34:35] nt
	s_add_u32 s34, s34, 0x2000
	s_addc_u32 s35, s35, 0
	global_load_dwordx4 v[32:35], v2, s[30:31] nt
	s_add_u32 s30, s30, 0x2000
	s_addc_u32 s31, s31, 0
	s_waitcnt vmcnt(14)
	global_store_dwordx4 v2, v[4:7], s[34:35] offset:-4096 nt
	s_nop 0
	global_load_dwordx4 v[4:7], v2, s[30:31] offset:-4096 nt
	s_waitcnt vmcnt(14)
	global_store_dwordx4 v2, v[8:11], s[34:35] nt
	s_add_u32 s34, s34, 0x2000
	s_addc_u32 s35, s35, 0
	global_load_dwordx4 v[8:11], v2, s[30:31] nt
	s_add_u32 s30, s30, 0x2000
	s_addc_u32 s31, s31, 0
	s_waitcnt vmcnt(14)
	global_store_dwordx4 v2, v[12:15], s[34:35] offset:-4096 nt
	s_nop 0
	global_load_dwordx4 v[12:15], v2, s[30:31] offset:-4096 nt
	s_waitcnt vmcnt(14)
	global_store_dwordx4 v2, v[16:19], s[34:35] nt
	s_add_u32 s34, s34, 0x2000
	s_addc_u32 s35, s35, 0
	global_load_dwordx4 v[16:19], v2, s[30:31] nt
	s_add_u32 s30, s30, 0x2000
	s_addc_u32 s31, s31, 0
	s_waitcnt vmcnt(14)
	global_store_dwordx4 v2, v[20:23], s[34:35] offset:-4096 nt
	s_nop 0
	global_load_dwordx4 v[20:23], v2, s[30:31] offset:-4096 nt
	s_waitcnt vmcnt(14)
	global_store_dwordx4 v2, v[24:27], s[34:35] nt
	s_add_u32 s34, s34, 0x2000
	s_addc_u32 s35, s35, 0
	global_load_dwordx4 v[24:27], v2, s[30:31] nt
	s_add_u32 s30, s30, 0x2000
	s_addc_u32 s31, s31, 0
	s_waitcnt vmcnt(14)
	global_store_dwordx4 v2, v[28:31], s[34:35] offset:-4096 nt
	s_nop 0
	global_load_dwordx4 v[28:31], v2, s[30:31] offset:-4096 nt
	s_waitcnt vmcnt(14)
	global_store_dwordx4 v2, v[32:35], s[34:35] nt
	s_add_u32 s34, s34, 0x2000
	s_addc_u32 s35, s35, 0
	global_load_dwordx4 v[32:35], v2, s[30:31] nt
	s_add_u32 s30, s30, 0x2000
	s_addc_u32 s31, s31, 0
	s_waitcnt vmcnt(14)
	global_store_dwordx4 v2, v[4:7], s[34:35] offset:-4096 nt
	s_nop 0
	global_load_dwordx4 v[4:7], v2, s[30:31] offset:-4096 nt
	s_waitcnt vmcnt(14)
	global_store_dwordx4 v2, v[8:11], s[34:35] nt
	s_add_u32 s34, s34, 0x2000
	s_addc_u32 s35, s35, 0
	global_load_dwordx4 v[8:11], v2, s[30:31] nt
	s_add_u32 s30, s30, 0x2000
	s_addc_u32 s31, s31, 0
	s_waitcnt vmcnt(14)
	global_store_dwordx4 v2, v[12:15], s[34:35] offset:-4096 nt
	s_nop 0
	global_load_dwordx4 v[12:15], v2, s[30:31] offset:-4096 nt
	s_waitcnt vmcnt(14)
	global_store_dwordx4 v2, v[16:19], s[34:35] nt
	s_add_u32 s34, s34, 0x2000
	s_addc_u32 s35, s35, 0
	global_load_dwordx4 v[16:19], v2, s[30:31] nt
	s_add_u32 s30, s30, 0x2000
	s_addc_u32 s31, s31, 0
	s_waitcnt vmcnt(14)
	global_store_dwordx4 v2, v[20:23], s[34:35] offset:-4096 nt
	s_nop 0
	global_load_dwordx4 v[20:23], v2, s[30:31] offset:-4096 nt
	s_waitcnt vmcnt(14)
	global_store_dwordx4 v2, v[24:27], s[34:35] nt
	s_add_u32 s34, s34, 0x2000
	s_addc_u32 s35, s35, 0
	global_load_dwordx4 v[24:27], v2, s[30:31] nt
	s_add_u32 s30, s30, 0x2000
	s_addc_u32 s31, s31, 0
	s_waitcnt vmcnt(14)
	global_store_dwordx4 v2, v[28:31], s[34:35] offset:-4096 nt
	s_nop 0
	global_load_dwordx4 v[28:31], v2, s[30:31] offset:-4096 nt
	s_waitcnt vmcnt(14)
	global_store_dwordx4 v2, v[32:35], s[34:35] nt
	s_add_u32 s34, s34, 0x2000
	s_addc_u32 s35, s35, 0
	global_load_dwordx4 v[32:35], v2, s[30:31] nt
	s_add_u32 s30, s30, 0x2000
	s_addc_u32 s31, s31, 0
	s_waitcnt vmcnt(14)
	global_store_dwordx4 v2, v[4:7], s[34:35] offset:-4096 nt
	s_nop 0
	global_load_dwordx4 v[4:7], v2, s[30:31] offset:-4096 nt
	s_waitcnt vmcnt(14)
	global_store_dwordx4 v2, v[8:11], s[34:35] nt
	s_add_u32 s34, s34, 0x2000
	s_addc_u32 s35, s35, 0
	global_load_dwordx4 v[8:11], v2, s[30:31] nt
	s_add_u32 s30, s30, 0x2000
	s_addc_u32 s31, s31, 0
	s_waitcnt vmcnt(14)
	global_store_dwordx4 v2, v[12:15], s[34:35] offset:-4096 nt
	s_nop 0
	global_load_dwordx4 v[12:15], v2, s[30:31] offset:-4096 nt
	s_waitcnt vmcnt(14)
	global_store_dwordx4 v2, v[16:19], s[34:35] nt
	s_add_u32 s34, s34, 0x2000
	s_addc_u32 s35, s35, 0
	global_load_dwordx4 v[16:19], v2, s[30:31] nt
	s_add_u32 s30, s30, 0x2000
	s_addc_u32 s31, s31, 0
	s_waitcnt vmcnt(14)
	global_store_dwordx4 v2, v[20:23], s[34:35] offset:-4096 nt
	s_nop 0
	global_load_dwordx4 v[20:23], v2, s[30:31] offset:-4096 nt
	s_waitcnt vmcnt(14)
	global_store_dwordx4 v2, v[24:27], s[34:35] nt
	s_add_u32 s34, s34, 0x2000
	s_addc_u32 s35, s35, 0
	global_load_dwordx4 v[24:27], v2, s[30:31] nt
	s_add_u32 s30, s30, 0x2000
	s_addc_u32 s31, s31, 0
	s_waitcnt vmcnt(14)
	global_store_dwordx4 v2, v[28:31], s[34:35] offset:-4096 nt
	s_nop 0
	global_load_dwordx4 v[28:31], v2, s[30:31] offset:-4096 nt
	s_waitcnt vmcnt(14)
	global_store_dwordx4 v2, v[32:35], s[34:35] nt
	s_add_u32 s34, s34, 0x2000
	s_addc_u32 s35, s35, 0
	global_load_dwordx4 v[32:35], v2, s[30:31] nt
	s_add_u32 s30, s30, 0x2000
	s_addc_u32 s31, s31, 0
	s_waitcnt vmcnt(14)
	global_store_dwordx4 v2, v[4:7], s[34:35] offset:-4096 nt
	s_nop 0
	global_load_dwordx4 v[4:7], v2, s[30:31] offset:-4096 nt
	s_waitcnt vmcnt(14)
	global_store_dwordx4 v2, v[8:11], s[34:35] nt
	s_add_u32 s34, s34, 0x2000
	s_addc_u32 s35, s35, 0
	global_load_dwordx4 v[8:11], v2, s[30:31] nt
	s_add_u32 s30, s30, 0x2000
	s_addc_u32 s31, s31, 0
	s_waitcnt vmcnt(14)
	global_store_dwordx4 v2, v[12:15], s[34:35] offset:-4096 nt
	s_nop 0
	global_load_dwordx4 v[12:15], v2, s[30:31] offset:-4096 nt
	s_waitcnt vmcnt(14)
	global_store_dwordx4 v2, v[16:19], s[34:35] nt
	s_add_u32 s34, s34, 0x2000
	s_addc_u32 s35, s35, 0
	global_load_dwordx4 v[16:19], v2, s[30:31] nt
	s_add_u32 s30, s30, 0x2000
	s_addc_u32 s31, s31, 0
	s_waitcnt vmcnt(14)
	global_store_dwordx4 v2, v[20:23], s[34:35] offset:-4096 nt
	s_nop 0
	global_load_dwordx4 v[20:23], v2, s[30:31] offset:-4096 nt
	s_waitcnt vmcnt(14)
	global_store_dwordx4 v2, v[24:27], s[34:35] nt
	s_add_u32 s34, s34, 0x2000
	s_addc_u32 s35, s35, 0
	global_load_dwordx4 v[24:27], v2, s[30:31] nt
	s_add_u32 s30, s30, 0x2000
	s_addc_u32 s31, s31, 0
	s_waitcnt vmcnt(14)
	global_store_dwordx4 v2, v[28:31], s[34:35] offset:-4096 nt
	s_nop 0
	global_load_dwordx4 v[28:31], v2, s[30:31] offset:-4096 nt
	s_waitcnt vmcnt(14)
	global_store_dwordx4 v2, v[32:35], s[34:35] nt
	s_add_u32 s34, s34, 0x2000
	s_addc_u32 s35, s35, 0
	global_load_dwordx4 v[32:35], v2, s[30:31] nt
	s_add_u32 s30, s30, 0x2000
	s_addc_u32 s31, s31, 0
	s_waitcnt vmcnt(14)
	global_store_dwordx4 v2, v[4:7], s[34:35] offset:-4096 nt
	s_nop 0
	s_waitcnt vmcnt(13)
	global_store_dwordx4 v2, v[8:11], s[34:35] nt
	s_add_u32 s34, s34, 0x2000
	s_addc_u32 s35, s35, 0
	s_waitcnt vmcnt(12)
	global_store_dwordx4 v2, v[12:15], s[34:35] offset:-4096 nt
	s_nop 0
	s_waitcnt vmcnt(11)
	global_store_dwordx4 v2, v[16:19], s[34:35] nt
	s_add_u32 s34, s34, 0x2000
	s_addc_u32 s35, s35, 0
	s_waitcnt vmcnt(10)
	global_store_dwordx4 v2, v[20:23], s[34:35] offset:-4096 nt
	s_nop 0
	s_waitcnt vmcnt(9)
	global_store_dwordx4 v2, v[24:27], s[34:35] nt
	s_add_u32 s34, s34, 0x2000
	s_addc_u32 s35, s35, 0
	s_waitcnt vmcnt(8)
	global_store_dwordx4 v2, v[28:31], s[34:35] offset:-4096 nt
	s_nop 0
	s_waitcnt vmcnt(7)
	global_store_dwordx4 v2, v[32:35], s[34:35] nt
	s_add_u32 s34, s34, 0x2000
	s_addc_u32 s35, s35, 0
	s_endpgm
